# PEER V second half, token end: counted vmcnt(16) (row prefetch stays in flight) when the token's own loads are older than the prefetch, full drain only when the token started in this batch or no prefe
# baseline (speedup 1.0000x reference)
.LBB0_1842:
	s_and_b64 s[38:39], s[6:7], exec
	s_cselect_b32 s52, s61, 0x80
	s_and_b64 s[38:39], s[40:41], exec
	s_cselect_b32 s52, s60, s52
	s_and_b64 s[38:39], s[42:43], exec
	s_cselect_b32 s39, s48, s52
	s_lshl_b32 s52, s57, 9
	s_add_i32 s52, s15, s52
	s_lshl_b32 s53, s59, 6
	s_add_i32 s52, s52, s53
	v_mov_b32_e32 v176, s52
	s_lshr_b32 s38, s39, 4
	s_add_i32 s70, s70, 1
	ds_read_b128 v[178:181], v176
	s_max_u32 s38, s38, s70
	s_lshl_b32 s48, s59, 4
	s_cmp_ge_i32 s48, s30
	s_cselect_b64 s[52:53], -1, 0
	s_cmp_lt_i32 s48, s39
	s_cselect_b64 s[54:55], -1, 0
	s_waitcnt lgkmcnt(0)
	s_and_b64 vcc, s[52:53], s[54:55]
	s_cselect_b32 s54, 0x45000000, 0
	v_mul_f32_e32 v1, s54, v178
	v_cvt_pk_fp8_f32 v2, v1, v1
	v_mul_f32_e32 v177, s54, v179
	v_cvt_pk_fp8_f32 v178, v177, v177
	v_perm_b32 v2, v2, v2, v249
	v_mov_b32_e32 v3, v0
	s_nop 1
	v_mfma_f32_16x16x32_fp8_fp8 v[160:163], v[2:3], v[4:5], v[160:163]
	v_mov_b32_e32 v1, v2
	v_mul_f32_e32 v177, s54, v180
	v_mfma_f32_16x16x32_fp8_fp8 v[152:155], v[2:3], v[6:7], v[152:155]
	v_perm_b32 v2, v178, v178, v249
	v_cvt_pk_fp8_f32 v178, v177, v177
	v_mfma_f32_16x16x32_fp8_fp8 v[164:167], v[0:1], v[4:5], v[164:167]
	v_mfma_f32_16x16x32_fp8_fp8 v[156:159], v[0:1], v[6:7], v[156:159]
	v_mov_b32_e32 v1, v2
	v_mfma_f32_16x16x32_fp8_fp8 v[160:163], v[2:3], v[8:9], v[160:163]
	v_mfma_f32_16x16x32_fp8_fp8 v[152:155], v[2:3], v[10:11], v[152:155]
	v_perm_b32 v2, v178, v178, v249
	s_nop 0
	s_nop 0
	v_mfma_f32_16x16x32_fp8_fp8 v[182:185], v[2:3], v[12:13], v[160:163]
	s_nop 1
	s_nop 1
	v_mul_f32_e32 v177, s54, v181
	v_cvt_pk_fp8_f32 v178, v177, v177
	v_mfma_f32_16x16x32_fp8_fp8 v[164:167], v[0:1], v[8:9], v[164:167]
	v_mfma_f32_16x16x32_fp8_fp8 v[156:159], v[0:1], v[10:11], v[156:159]
	v_mov_b32_e32 v1, v2
	v_mfma_f32_16x16x32_fp8_fp8 v[160:163], v[2:3], v[14:15], v[152:155]
	v_perm_b32 v2, v178, v178, v249
	ds_read_b128 v[178:181], v176 offset:16
	v_mfma_f32_16x16x32_fp8_fp8 v[164:167], v[0:1], v[12:13], v[164:167]
	s_waitcnt lgkmcnt(0)
	v_mul_f32_e32 v177, s54, v178
	v_cvt_pk_fp8_f32 v178, v177, v177
	v_mfma_f32_16x16x32_fp8_fp8 v[156:159], v[0:1], v[14:15], v[156:159]
	v_mov_b32_e32 v1, v2
	v_mfma_f32_16x16x32_fp8_fp8 v[152:155], v[2:3], v[16:17], v[182:185]
	v_mul_f32_e32 v177, s54, v179
	v_mfma_f32_16x16x32_fp8_fp8 v[160:163], v[2:3], v[18:19], v[160:163]
	v_perm_b32 v2, v178, v178, v249
	v_cvt_pk_fp8_f32 v178, v177, v177
	v_mfma_f32_16x16x32_fp8_fp8 v[164:167], v[0:1], v[16:17], v[164:167]
	v_mul_f32_e32 v177, s54, v180
	v_mfma_f32_16x16x32_fp8_fp8 v[156:159], v[0:1], v[18:19], v[156:159]
	v_mov_b32_e32 v1, v2
	v_mfma_f32_16x16x32_fp8_fp8 v[152:155], v[2:3], v[20:21], v[152:155]
	v_mfma_f32_16x16x32_fp8_fp8 v[160:163], v[2:3], v[22:23], v[160:163]
	v_perm_b32 v2, v178, v178, v249
	v_cvt_pk_fp8_f32 v178, v177, v177
	v_mfma_f32_16x16x32_fp8_fp8 v[164:167], v[0:1], v[20:21], v[164:167]
	v_mfma_f32_16x16x32_fp8_fp8 v[156:159], v[0:1], v[22:23], v[156:159]
	v_mov_b32_e32 v1, v2
	v_mul_f32_e32 v177, s54, v181
	v_mfma_f32_16x16x32_fp8_fp8 v[152:155], v[2:3], v[24:25], v[152:155]
	v_mfma_f32_16x16x32_fp8_fp8 v[160:163], v[2:3], v[26:27], v[160:163]
	v_perm_b32 v2, v178, v178, v249
	v_cvt_pk_fp8_f32 v178, v177, v177
	v_mfma_f32_16x16x32_fp8_fp8 v[164:167], v[0:1], v[24:25], v[164:167]
	v_mfma_f32_16x16x32_fp8_fp8 v[156:159], v[0:1], v[26:27], v[156:159]
	v_mov_b32_e32 v1, v2
	v_mfma_f32_16x16x32_fp8_fp8 v[152:155], v[2:3], v[28:29], v[152:155]
	v_mfma_f32_16x16x32_fp8_fp8 v[160:163], v[2:3], v[30:31], v[160:163]
	v_perm_b32 v2, v178, v178, v249
	ds_read_b128 v[178:181], v176 offset:32
	s_waitcnt lgkmcnt(0)
	v_mul_f32_e32 v177, s54, v178
	v_cvt_pk_fp8_f32 v178, v177, v177
	v_mfma_f32_16x16x32_fp8_fp8 v[164:167], v[0:1], v[28:29], v[164:167]
	v_mfma_f32_16x16x32_fp8_fp8 v[156:159], v[0:1], v[30:31], v[156:159]
	v_mov_b32_e32 v1, v2
	v_mul_f32_e32 v177, s54, v179
	v_mfma_f32_16x16x32_fp8_fp8 v[152:155], v[2:3], v[32:33], v[152:155]
	v_mfma_f32_16x16x32_fp8_fp8 v[160:163], v[2:3], v[34:35], v[160:163]
	v_perm_b32 v2, v178, v178, v249
	v_cvt_pk_fp8_f32 v178, v177, v177
	v_mfma_f32_16x16x32_fp8_fp8 v[164:167], v[0:1], v[32:33], v[164:167]
	v_mfma_f32_16x16x32_fp8_fp8 v[156:159], v[0:1], v[34:35], v[156:159]
	v_mov_b32_e32 v1, v2
	v_mul_f32_e32 v177, s54, v180
	v_mfma_f32_16x16x32_fp8_fp8 v[152:155], v[2:3], v[36:37], v[152:155]
	v_mfma_f32_16x16x32_fp8_fp8 v[160:163], v[2:3], v[38:39], v[160:163]
	v_perm_b32 v2, v178, v178, v249
	v_cvt_pk_fp8_f32 v178, v177, v177
	v_mfma_f32_16x16x32_fp8_fp8 v[164:167], v[0:1], v[36:37], v[164:167]
	v_mfma_f32_16x16x32_fp8_fp8 v[156:159], v[0:1], v[38:39], v[156:159]
	v_mov_b32_e32 v1, v2
	v_mul_f32_e32 v177, s54, v181
	v_mfma_f32_16x16x32_fp8_fp8 v[152:155], v[2:3], v[40:41], v[152:155]
	v_mfma_f32_16x16x32_fp8_fp8 v[160:163], v[2:3], v[42:43], v[160:163]
	v_perm_b32 v2, v178, v178, v249
	v_cvt_pk_fp8_f32 v178, v177, v177
	v_mfma_f32_16x16x32_fp8_fp8 v[164:167], v[0:1], v[40:41], v[164:167]
	v_mfma_f32_16x16x32_fp8_fp8 v[156:159], v[0:1], v[42:43], v[156:159]
	v_mov_b32_e32 v1, v2
	v_mfma_f32_16x16x32_fp8_fp8 v[152:155], v[2:3], v[44:45], v[152:155]
	v_mfma_f32_16x16x32_fp8_fp8 v[160:163], v[2:3], v[46:47], v[160:163]
	v_perm_b32 v2, v178, v178, v249
	ds_read_b128 v[176:179], v176 offset:48
	v_mfma_f32_16x16x32_fp8_fp8 v[164:167], v[0:1], v[44:45], v[164:167]
	s_waitcnt lgkmcnt(0)
	v_mul_f32_e32 v176, s54, v176
	v_cvt_pk_fp8_f32 v180, v176, v176
	v_mfma_f32_16x16x32_fp8_fp8 v[156:159], v[0:1], v[46:47], v[156:159]
	v_mov_b32_e32 v1, v2
	v_mul_f32_e32 v176, s54, v177
	v_cvt_pk_fp8_f32 v177, v176, v176
	v_mfma_f32_16x16x32_fp8_fp8 v[152:155], v[2:3], v[48:49], v[152:155]
	v_mfma_f32_16x16x32_fp8_fp8 v[160:163], v[2:3], v[50:51], v[160:163]
	v_perm_b32 v2, v180, v180, v249
	v_mfma_f32_16x16x32_fp8_fp8 v[164:167], v[0:1], v[48:49], v[164:167]
	v_mul_f32_e32 v176, s54, v178
	v_mfma_f32_16x16x32_fp8_fp8 v[156:159], v[0:1], v[50:51], v[156:159]
	v_mov_b32_e32 v1, v2
	v_mfma_f32_16x16x32_fp8_fp8 v[152:155], v[2:3], v[52:53], v[152:155]
	s_add_i32 s38, s38, -1
	v_mfma_f32_16x16x32_fp8_fp8 v[160:163], v[2:3], v[54:55], v[160:163]
	v_perm_b32 v2, v177, v177, v249
	v_cvt_pk_fp8_f32 v177, v176, v176
	v_mfma_f32_16x16x32_fp8_fp8 v[164:167], v[0:1], v[52:53], v[164:167]
	s_cmp_lg_u32 s59, s38
	v_mfma_f32_16x16x32_fp8_fp8 v[156:159], v[0:1], v[54:55], v[156:159]
	v_mov_b32_e32 v1, v2
	v_mul_f32_e32 v180, s54, v179
	v_cvt_pk_fp8_f32 v181, v180, v180
	v_mfma_f32_16x16x32_fp8_fp8 v[152:155], v[2:3], v[56:57], v[152:155]
	v_mfma_f32_16x16x32_fp8_fp8 v[160:163], v[2:3], v[58:59], v[160:163]
	v_perm_b32 v2, v177, v177, v249
	v_mfma_f32_16x16x32_fp8_fp8 v[164:167], v[0:1], v[56:57], v[164:167]
	v_mfma_f32_16x16x32_fp8_fp8 v[156:159], v[0:1], v[58:59], v[156:159]
	v_mov_b32_e32 v1, v2
	v_mfma_f32_16x16x32_fp8_fp8 v[152:155], v[2:3], v[60:61], v[152:155]
	v_mfma_f32_16x16x32_fp8_fp8 v[176:179], v[2:3], v[62:63], v[160:163]
	v_perm_b32 v2, v181, v181, v249
	v_mfma_f32_16x16x32_fp8_fp8 v[164:167], v[0:1], v[60:61], v[164:167]
	v_mfma_f32_16x16x32_fp8_fp8 v[156:159], v[0:1], v[62:63], v[156:159]
	v_mov_b32_e32 v1, v2
	v_mfma_f32_16x16x32_fp8_fp8 v[160:163], v[2:3], v[64:65], v[152:155]
	s_nop 0
	v_mfma_f32_16x16x32_fp8_fp8 v[164:167], v[0:1], v[64:65], v[164:167]
	v_mfma_f32_16x16x32_fp8_fp8 v[152:155], v[2:3], v[66:67], v[176:179]
	v_mfma_f32_16x16x32_fp8_fp8 v[156:159], v[0:1], v[66:67], v[156:159]
	s_cbranch_scc1 .LBB0_1850
	s_add_i32 s30, s59, 1
	s_cmp_eq_u32 s30, s70
	s_cbranch_scc1 .Lpv_te_drain
	s_cmp_gt_i32 s58, 15
	s_cbranch_scc1 .Lpv_te_drain
	s_waitcnt vmcnt(16)
	s_branch .Lpv_te_go

; __device__ __forceinline__ void peer_token_end(Frame& F, const Args& a, int layer, bool last, bool final_half, size_t tok, int lane, const f32x2 (&out)[8], const f32x4 (&hpre)[4], const v4u (&gpre)[2], const v4u& p8pre) {
;     float* hp = F.h + tok * 1024 + 16 * lane;
;     f32x4 hv[4], ge[4]; float s = 0.f;
;     f32x4 pe[4];
; #pragma unroll
;     for (int i = 0; i < 4; ++i) { const f32x2 lo = __builtin_amdgcn_cvt_pk_f32_fp8((int)p8pre[i], false), hi = __builtin_amdgcn_cvt_pk_f32_fp8((int)p8pre[i], true);
;         pe[i] = (f32x4){lo.x, lo.y, hi.x, hi.y} * (1.f / 256.f) + (f32x4){out[2 * i].x, out[2 * i].y, out[2 * i + 1].x, out[2 * i + 1].y}; }
;     if (!final_half) {
;         v4u w;
; #pragma unroll
;         for (int i = 0; i < 4; ++i) { const f32x4 s8 = pe[i] * 256.f; int t = 0; t = __builtin_amdgcn_cvt_pk_fp8_f32(s8.x, s8.y, t, false); t = __builtin_amdgcn_cvt_pk_fp8_f32(s8.z, s8.w, t, true); w[i] = (unsigned)t; }
;         *(v4u*)((unsigned char*)(F.ws + WS_P8) + tok * 1024 + 16 * lane) = w;
;         return; }
.Lpv_te_go:
	v_cvt_pk_f32_fp8_e32 v[2:3], v140
	v_cvt_pk_f32_fp8_e32 v[178:179], v141
	v_cvt_pk_f32_fp8_sdwa v[180:181], v141 src0_sel:WORD_1
	v_cvt_pk_f32_fp8_sdwa v[188:189], v142 src0_sel:WORD_1
	v_pk_mul_f32 v[2:3], v[2:3], s[12:13] op_sel_hi:[1,0]
	v_cvt_pk_f32_fp8_e32 v[186:187], v142
	v_pk_fma_f32 v[182:183], v[160:161], s[14:15], v[2:3] op_sel_hi:[1,0,1]
	v_pk_mul_f32 v[2:3], v[178:179], s[12:13] op_sel_hi:[1,0]
	v_pk_mul_f32 v[178:179], v[180:181], s[12:13] op_sel_hi:[1,0]
	v_cvt_pk_f32_fp8_sdwa v[176:177], v140 src0_sel:WORD_1
	v_pk_fma_f32 v[180:181], v[166:167], s[14:15], v[178:179] op_sel_hi:[1,0,1]
	v_pk_mul_f32 v[178:179], v[188:189], s[12:13] op_sel_hi:[1,0]
	v_cvt_pk_f32_fp8_e32 v[188:189], v143
	v_cvt_pk_f32_fp8_sdwa v[192:193], v143 src0_sel:WORD_1
	s_ashr_i32 s30, s57, 31
	s_add_u32 s52, s0, s57
	v_pk_fma_f32 v[184:185], v[164:165], s[14:15], v[2:3] op_sel_hi:[1,0,1]
	v_pk_mul_f32 v[2:3], v[186:187], s[12:13] op_sel_hi:[1,0]
	s_addc_u32 s53, s1, s30
	v_pk_mul_f32 v[176:177], v[176:177], s[12:13] op_sel_hi:[1,0]
	v_pk_fma_f32 v[186:187], v[154:155], s[14:15], v[178:179] op_sel_hi:[1,0,1]
	v_pk_fma_f32 v[190:191], v[152:153], s[14:15], v[2:3] op_sel_hi:[1,0,1]
	v_pk_mul_f32 v[2:3], v[188:189], s[12:13] op_sel_hi:[1,0]
	v_pk_mul_f32 v[178:179], v[192:193], s[12:13] op_sel_hi:[1,0]
	s_lshl_b64 s[38:39], s[52:53], 10
	v_pk_fma_f32 v[176:177], v[162:163], s[14:15], v[176:177] op_sel_hi:[1,0,1]
	v_pk_fma_f32 v[188:189], v[158:159], s[14:15], v[178:179] op_sel_hi:[1,0,1]
	v_pk_fma_f32 v[192:193], v[156:157], s[14:15], v[2:3] op_sel_hi:[1,0,1]
	s_andn2_b64 vcc, exec, s[46:47]
	s_mov_b64 s[54:55], -1
	s_cbranch_vccnz .LBB0_1845
	v_pk_mul_f32 v[2:3], v[182:183], s[8:9] op_sel_hi:[1,0]
	v_mov_b32_e32 v194, v0
	v_cvt_pk_fp8_f32 v194, v2, v3
	v_pk_mul_f32 v[2:3], v[184:185], s[8:9] op_sel_hi:[1,0]
	v_mov_b32_e32 v195, v0
	v_cvt_pk_fp8_f32 v195, v2, v3
	v_pk_mul_f32 v[2:3], v[176:177], s[8:9] op_sel_hi:[1,0]
	v_mov_b32_e32 v196, v0
	v_cvt_pk_fp8_f32 v194, v2, v3 op_sel:[0,0,1]
	v_pk_mul_f32 v[2:3], v[180:181], s[8:9] op_sel_hi:[1,0]
	v_mov_b32_e32 v197, v0
	v_cvt_pk_fp8_f32 v195, v2, v3 op_sel:[0,0,1]
	v_pk_mul_f32 v[2:3], v[190:191], s[8:9] op_sel_hi:[1,0]
	s_mov_b64 s[54:55], 0
	v_cvt_pk_fp8_f32 v196, v2, v3
	v_pk_mul_f32 v[2:3], v[192:193], s[8:9] op_sel_hi:[1,0]
	s_nop 0
	v_cvt_pk_fp8_f32 v197, v2, v3
	v_pk_mul_f32 v[2:3], v[186:187], s[8:9] op_sel_hi:[1,0]
	s_nop 0
	v_cvt_pk_fp8_f32 v196, v2, v3 op_sel:[0,0,1]
	v_pk_mul_f32 v[2:3], v[188:189], s[8:9] op_sel_hi:[1,0]
	s_nop 0
	v_cvt_pk_fp8_f32 v197, v2, v3 op_sel:[0,0,1]
	v_lshl_add_u64 v[2:3], v[234:235], 0, s[38:39]
	global_store_dwordx4 v[2:3], v[194:197], off
